# weight-conversion loops: nt (streaming) hint on the read-once f32 weight loads and sc1 write-through on the tile-loop stores, so the 1 GB weight stream stops evicting GEMM operands from L2/MALL; plus
# speedup vs baseline: 1.0215x; 1.0182x over previous
.LBB0_9:
	s_add_u32 s48, s70, 0x11000000
	s_addc_u32 s49, s71, 0
	s_add_u32 s50, s70, 0x780000
	s_addc_u32 s51, s71, 0
	s_ashr_i32 s2, s5, 6
	s_mul_i32 s5, s4, 0x1ffc
	s_or_b32 s10, s5, 0x80
	s_lshl_b32 s22, s2, 8
	s_lshl_b32 s53, s2, 10
	s_cmp_eq_u64 s[0:1], 0
	s_cselect_b64 s[20:21], -1, 0
	v_and_b32_e32 v128, 63, v134
	s_and_b64 s[24:25], s[20:21], exec
	s_cselect_b32 s1, s63, s1
	s_cselect_b32 s0, s62, s0
	v_or_b32_e32 v136, s22, v128
	v_mov_b32_e32 v0, s0
	v_mov_b32_e32 v1, s1
	v_ashrrev_i32_e32 v137, 31, v136
	v_lshl_add_u64 v[0:1], v[136:137], 2, v[0:1]
	v_bfe_u32 v133, v134, 3, 3
	v_lshlrev_b32_e32 v140, 2, v134
	global_load_dword v130, v[0:1], off
	global_load_dword v131, v[0:1], off offset:256
	global_load_dword v138, v[0:1], off offset:512
	global_load_dword v139, v[0:1], off offset:768
	v_mul_u32_u24_e32 v0, s4, v133
	v_and_b32_e32 v142, 28, v140
	v_or_b32_e32 v0, v0, v142
	s_mul_i32 s0, s4, s53
	s_lshl_b32 s1, s4, 5
	s_mov_b32 s11, 0x20000
	v_lshlrev_b32_e32 v0, 2, v0
	s_and_b32 s9, s9, 0xffff
	s_add_i32 s4, s0, s1
	buffer_load_dwordx4 v[124:127], v0, s[8:11], s0 offen nt
	buffer_load_dwordx4 v[120:123], v0, s[8:11], s4 offen nt
	s_add_i32 s0, s4, s1
	s_add_i32 s4, s0, s1
	buffer_load_dwordx4 v[116:119], v0, s[8:11], s0 offen nt
	buffer_load_dwordx4 v[112:115], v0, s[8:11], s4 offen nt
	s_add_i32 s0, s4, s1
	s_add_i32 s4, s0, s1
	buffer_load_dwordx4 v[108:111], v0, s[8:11], s0 offen nt
	buffer_load_dwordx4 v[104:107], v0, s[8:11], s4 offen nt
	s_add_i32 s0, s4, s1
	s_add_i32 s4, s0, s1
	buffer_load_dwordx4 v[100:103], v0, s[8:11], s0 offen nt
	buffer_load_dwordx4 v[92:95], v0, s[8:11], s4 offen nt
	s_add_i32 s0, s4, s1
	s_add_i32 s4, s0, s1
	s_add_i32 s5, s4, s1
	s_add_i32 s23, s5, s1
	s_add_i32 s24, s23, s1
	s_add_i32 s25, s24, s1
	s_add_i32 s26, s25, s1
	s_add_i32 s27, s26, s1
	s_add_i32 s30, s27, s1
	s_add_i32 s31, s30, s1
	s_add_i32 s34, s31, s1
	s_add_i32 s35, s34, s1
	s_add_i32 s36, s35, s1
	s_add_i32 s37, s36, s1
	s_add_i32 s38, s37, s1
	s_add_i32 s39, s38, s1
	s_add_i32 s40, s39, s1
	s_add_i32 s41, s40, s1
	s_add_i32 s42, s41, s1
	s_add_i32 s43, s42, s1
	s_add_i32 s54, s43, s1
	s_mov_b32 s79, s55
	s_add_i32 s55, s54, s1
	s_add_i32 s72, s55, s1
	s_add_i32 s1, s72, s1
	buffer_load_dwordx4 v[96:99], v0, s[8:11], s0 offen nt
	buffer_load_dwordx4 v[88:91], v0, s[8:11], s4 offen nt
	buffer_load_dwordx4 v[84:87], v0, s[8:11], s5 offen nt
	buffer_load_dwordx4 v[80:83], v0, s[8:11], s23 offen nt
	buffer_load_dwordx4 v[76:79], v0, s[8:11], s24 offen nt
	buffer_load_dwordx4 v[72:75], v0, s[8:11], s25 offen nt
	buffer_load_dwordx4 v[68:71], v0, s[8:11], s26 offen nt
	buffer_load_dwordx4 v[64:67], v0, s[8:11], s27 offen nt
	buffer_load_dwordx4 v[60:63], v0, s[8:11], s30 offen nt
	buffer_load_dwordx4 v[56:59], v0, s[8:11], s31 offen nt
	buffer_load_dwordx4 v[52:55], v0, s[8:11], s34 offen nt
	buffer_load_dwordx4 v[48:51], v0, s[8:11], s35 offen nt
	buffer_load_dwordx4 v[44:47], v0, s[8:11], s36 offen nt
	buffer_load_dwordx4 v[40:43], v0, s[8:11], s37 offen nt
	buffer_load_dwordx4 v[36:39], v0, s[8:11], s38 offen nt
	buffer_load_dwordx4 v[32:35], v0, s[8:11], s39 offen nt
	buffer_load_dwordx4 v[28:31], v0, s[8:11], s40 offen nt
	buffer_load_dwordx4 v[24:27], v0, s[8:11], s41 offen nt
	buffer_load_dwordx4 v[20:23], v0, s[8:11], s42 offen nt
	buffer_load_dwordx4 v[16:19], v0, s[8:11], s43 offen nt
	buffer_load_dwordx4 v[12:15], v0, s[8:11], s54 offen nt
	buffer_load_dwordx4 v[8:11], v0, s[8:11], s55 offen nt
	buffer_load_dwordx4 v[4:7], v0, s[8:11], s72 offen nt
	s_nop 0
	buffer_load_dwordx4 v[0:3], v0, s[8:11], s1 offen nt
	v_mbcnt_lo_u32_b32 v141, -1, 0
	v_cndmask_b32_e64 v129, 1.0, 0, s[20:21]
	v_mbcnt_hi_u32_b32 v141, -1, v141
	v_cndmask_b32_e64 v161, 0, 1.0, s[20:21]
	v_cmp_gt_u32_e64 s[4:5], 8, v128
	v_lshlrev_b32_e32 v143, 4, v128
	v_or_b32_e32 v148, s22, v133
	v_mul_u32_u24_e32 v147, 0x1008, v142
	s_lshl_b32 s8, s2, 7
	s_add_i32 s9, 0, 0x22400
	s_add_i32 s54, s9, s8
	s_lshl_b32 s8, s2, 2
	v_add_u32_e32 v144, s9, v140
	s_ashr_i32 s9, s8, 31
	s_lshl_b32 s10, s2, 4
	s_mulk_i32 s2, 0x4020
	s_or_b32 s22, s8, 1
	s_add_i32 s72, s2, 0
	s_lshl_b64 s[20:21], s[8:9], 11
	s_mul_i32 s2, s22, 0x1008
	s_or_b32 s24, s8, 2
	s_or_b32 s8, s8, 3
	s_add_i32 s55, 0, 0x22800
	s_ashr_i32 s23, s22, 31
	s_add_i32 s73, s2, 0
	s_ashr_i32 s25, s24, 31
	s_ashr_i32 s9, s8, 31
	v_cmp_gt_i32_e64 s[0:1], 32, v134
	v_ashrrev_i32_e32 v135, 31, v134
	v_add_u32_e32 v145, s55, v140
	s_add_i32 s55, s55, s10
	s_waitcnt vmcnt(35)
	v_fma_f32 v164, v129, v130, v161
	s_waitcnt vmcnt(34)
	v_fma_f32 v163, v129, v131, v161
	s_waitcnt vmcnt(33)
	v_fma_f32 v162, v129, v138, v161
	v_lshlrev_b32_e32 v138, 3, v128
	v_and_b32_e32 v128, 64, v141
	s_waitcnt vmcnt(32)
	v_fmac_f32_e32 v161, v129, v139
	v_or_b32_e32 v129, v128, v133
	v_lshlrev_b32_e32 v146, 2, v129
	v_lshlrev_b32_e32 v129, 1, v148
	v_add3_u32 v147, 0, v147, v129
	v_xor_b32_e32 v129, 8, v141
	v_add_u32_e32 v128, 64, v128
	v_cmp_lt_i32_e32 vcc, v129, v128
	v_or_b32_e32 v148, 32, v146
	v_or_b32_e32 v149, 64, v146
	v_cndmask_b32_e32 v129, v141, v129, vcc
	v_lshlrev_b32_e32 v155, 2, v129
	v_xor_b32_e32 v129, 16, v141
	v_cmp_lt_i32_e32 vcc, v129, v128
	v_or_b32_e32 v150, 0x60, v146
	v_or_b32_e32 v151, 0x80, v146
	v_cndmask_b32_e32 v129, v141, v129, vcc
	v_lshlrev_b32_e32 v156, 2, v129
	v_xor_b32_e32 v129, 32, v141
	v_cmp_lt_i32_e32 vcc, v129, v128
	v_or_b32_e32 v152, 0xa0, v146
	v_or_b32_e32 v153, 0xc0, v146
	v_cndmask_b32_e32 v128, v141, v129, vcc
	v_or_b32_e32 v154, 0xe0, v146
	v_lshlrev_b32_e32 v157, 2, v128
	v_mov_b32_e32 v139, 0
	v_or_b32_e32 v158, 0x400, v143
	v_or_b32_e32 v159, 0x800, v143
	v_or_b32_e32 v160, 0xc00, v143
	s_lshl_b64 s[22:23], s[22:23], 11
	s_add_i32 s74, s73, 0x1008
	s_lshl_b64 s[24:25], s[24:25], 11
	s_add_i32 s75, s73, 0x2010
	s_lshl_b64 s[26:27], s[8:9], 11
	s_mov_b32 s76, 0xda24260
	s_mov_b32 s77, 0x42fe0000
	s_mov_b32 s78, 0x40c0c00
	s_mov_b32 s2, s79
	s_branch .LBB0_11

.LBB0_37:
	s_mul_i32 s10, s2, 0x1ffc
	s_bitset1_b32 s10, 7
	s_and_b64 s[38:39], s[38:39], exec
	s_cselect_b32 s10, s10, 0
	s_cmp_eq_u64 s[40:41], 0
	s_cselect_b64 s[38:39], -1, 0
	v_readlane_b32 s56, v252, 24
	s_and_b64 s[42:43], s[38:39], exec
	v_readlane_b32 s62, v252, 30
	v_readlane_b32 s63, v252, 31
	v_mul_u32_u24_e32 v0, s2, v133
	s_cselect_b32 s41, s63, s41
	s_cselect_b32 s40, s62, s40
	v_or_b32_e32 v2, v0, v142
	v_mov_b32_e32 v0, s40
	v_mov_b32_e32 v1, s41
	s_mul_i32 s80, s2, s53
	v_lshl_add_u64 v[0:1], v[136:137], 2, v[0:1]
	s_lshl_b32 s2, s2, 5
	global_load_dword v162, v[0:1], off
	global_load_dword v140, v[0:1], off offset:256
	global_load_dword v141, v[0:1], off offset:512
	global_load_dword v165, v[0:1], off offset:768
	s_and_b32 s9, s9, 0xffff
	v_lshlrev_b32_e32 v0, 2, v2
	s_add_i32 s40, s80, s2
	buffer_load_dwordx4 v[124:127], v0, s[8:11], s80 offen nt
	buffer_load_dwordx4 v[120:123], v0, s[8:11], s40 offen nt
	s_add_i32 s40, s40, s2
	s_add_i32 s41, s40, s2
	buffer_load_dwordx4 v[116:119], v0, s[8:11], s40 offen nt
	buffer_load_dwordx4 v[112:115], v0, s[8:11], s41 offen nt
	s_add_i32 s40, s41, s2
	s_add_i32 s41, s40, s2
	buffer_load_dwordx4 v[108:111], v0, s[8:11], s40 offen nt
	buffer_load_dwordx4 v[104:107], v0, s[8:11], s41 offen nt
	s_add_i32 s40, s41, s2
	s_add_i32 s41, s40, s2
	buffer_load_dwordx4 v[100:103], v0, s[8:11], s40 offen nt
	buffer_load_dwordx4 v[92:95], v0, s[8:11], s41 offen nt
	s_add_i32 s40, s41, s2
	s_add_i32 s41, s40, s2
	buffer_load_dwordx4 v[96:99], v0, s[8:11], s40 offen nt
	buffer_load_dwordx4 v[88:91], v0, s[8:11], s41 offen nt
	s_add_i32 s40, s41, s2
	s_add_i32 s41, s40, s2
	buffer_load_dwordx4 v[84:87], v0, s[8:11], s40 offen nt
	buffer_load_dwordx4 v[80:83], v0, s[8:11], s41 offen nt
	s_add_i32 s40, s41, s2
	s_add_i32 s41, s40, s2
	buffer_load_dwordx4 v[76:79], v0, s[8:11], s40 offen nt
	buffer_load_dwordx4 v[72:75], v0, s[8:11], s41 offen nt
	s_add_i32 s40, s41, s2
	s_add_i32 s41, s40, s2
	buffer_load_dwordx4 v[68:71], v0, s[8:11], s40 offen nt
	buffer_load_dwordx4 v[64:67], v0, s[8:11], s41 offen nt
	s_add_i32 s40, s41, s2
	s_add_i32 s41, s40, s2
	buffer_load_dwordx4 v[60:63], v0, s[8:11], s40 offen nt
	buffer_load_dwordx4 v[56:59], v0, s[8:11], s41 offen nt
	s_add_i32 s40, s41, s2
	s_add_i32 s41, s40, s2
	buffer_load_dwordx4 v[52:55], v0, s[8:11], s40 offen nt
	buffer_load_dwordx4 v[48:51], v0, s[8:11], s41 offen nt
	s_add_i32 s40, s41, s2
	s_add_i32 s41, s40, s2
	buffer_load_dwordx4 v[44:47], v0, s[8:11], s40 offen nt
	buffer_load_dwordx4 v[40:43], v0, s[8:11], s41 offen nt
	s_add_i32 s40, s41, s2
	s_add_i32 s41, s40, s2
	buffer_load_dwordx4 v[36:39], v0, s[8:11], s40 offen nt
	buffer_load_dwordx4 v[32:35], v0, s[8:11], s41 offen nt
	s_add_i32 s40, s41, s2
	s_add_i32 s41, s40, s2
	buffer_load_dwordx4 v[28:31], v0, s[8:11], s40 offen nt
	buffer_load_dwordx4 v[24:27], v0, s[8:11], s41 offen nt
	s_add_i32 s40, s41, s2
	s_add_i32 s41, s40, s2
	buffer_load_dwordx4 v[20:23], v0, s[8:11], s40 offen nt
	buffer_load_dwordx4 v[16:19], v0, s[8:11], s41 offen nt
	s_add_i32 s40, s41, s2
	s_add_i32 s41, s40, s2
	buffer_load_dwordx4 v[12:15], v0, s[8:11], s40 offen nt
	buffer_load_dwordx4 v[8:11], v0, s[8:11], s41 offen nt
	s_add_i32 s40, s41, s2
	s_add_i32 s2, s40, s2
	buffer_load_dwordx4 v[4:7], v0, s[8:11], s40 offen nt
	s_nop 0
	buffer_load_dwordx4 v[0:3], v0, s[8:11], s2 offen nt
	v_readlane_b32 s57, v252, 25
	v_readlane_b32 s58, v252, 26
	v_readlane_b32 s59, v252, 27
	v_readlane_b32 s60, v252, 28
	v_readlane_b32 s61, v252, 29
	v_readlane_b32 s64, v252, 32
	v_readlane_b32 s65, v252, 33
	v_readlane_b32 s66, v252, 34
	v_readlane_b32 s67, v252, 35
	v_readlane_b32 s68, v252, 36
	v_readlane_b32 s69, v252, 37
	v_readlane_b32 s70, v252, 38
	v_readlane_b32 s71, v252, 39
	s_and_saveexec_b64 s[8:9], s[0:1]
	s_cbranch_execz .LBB0_10
	ds_read2_b32 v[128:129], v144 offset1:32
	ds_read2_b32 v[130:131], v144 offset0:64 offset1:96
	ds_read2_b32 v[166:167], v144 offset0:128 offset1:160
	ds_read2_b32 v[168:169], v144 offset0:192 offset1:224
	s_waitcnt lgkmcnt(3)
	v_max3_f32 v128, v128, s76, v129
	s_waitcnt lgkmcnt(2)
	v_max3_f32 v128, v128, v130, v131
	s_waitcnt lgkmcnt(1)
	v_max3_f32 v128, v128, v166, v167
	s_waitcnt lgkmcnt(0)
	v_max3_f32 v128, v128, v168, v169
	ds_write_b32 v145, v128
	v_mul_f32_e32 v130, 0x3c010204, v128
	v_lshl_add_u64 v[128:129], v[134:135], 2, s[28:29]
	global_store_dword v[128:129], v130, off
	s_branch .LBB0_10

.LBB0_67:
	s_ashr_i32 s4, s10, 6
	s_mul_i32 s5, s7, 0x1fc
	s_or_b32 s10, s5, 0x400
	s_lshl_b32 s36, s4, 4
	s_lshl_b32 s5, s7, 2
	v_and_b32_e32 v70, 63, v0
	s_mul_i32 s6, s5, s36
	s_and_b32 s9, s9, 0xffff
	s_mov_b32 s11, 0x20000
	v_lshlrev_b32_e32 v71, 4, v70
	s_add_i32 s7, s6, s5
	buffer_load_dwordx4 v[0:3], v71, s[8:11], s6 offen nt
	buffer_load_dwordx4 v[4:7], v71, s[8:11], s7 offen nt
	s_add_i32 s6, s7, s5
	s_add_i32 s7, s6, s5
	buffer_load_dwordx4 v[8:11], v71, s[8:11], s6 offen nt
	buffer_load_dwordx4 v[12:15], v71, s[8:11], s7 offen nt
	s_add_i32 s6, s7, s5
	s_add_i32 s7, s6, s5
	buffer_load_dwordx4 v[16:19], v71, s[8:11], s6 offen nt
	buffer_load_dwordx4 v[20:23], v71, s[8:11], s7 offen nt
	s_add_i32 s6, s7, s5
	s_add_i32 s7, s6, s5
	buffer_load_dwordx4 v[24:27], v71, s[8:11], s6 offen nt
	buffer_load_dwordx4 v[28:31], v71, s[8:11], s7 offen nt
	s_add_i32 s6, s7, s5
	s_add_i32 s7, s6, s5
	buffer_load_dwordx4 v[32:35], v71, s[8:11], s6 offen nt
	buffer_load_dwordx4 v[36:39], v71, s[8:11], s7 offen nt
	s_add_i32 s6, s7, s5
	s_add_i32 s7, s6, s5
	buffer_load_dwordx4 v[40:43], v71, s[8:11], s6 offen nt
	buffer_load_dwordx4 v[44:47], v71, s[8:11], s7 offen nt
	s_add_i32 s6, s7, s5
	s_add_i32 s7, s6, s5
	buffer_load_dwordx4 v[48:51], v71, s[8:11], s6 offen nt
	buffer_load_dwordx4 v[52:55], v71, s[8:11], s7 offen nt
	s_add_i32 s6, s7, s5
	s_add_i32 s5, s6, s5
	buffer_load_dwordx4 v[56:59], v71, s[8:11], s6 offen nt
	buffer_load_dwordx4 v[60:63], v71, s[8:11], s5 offen nt
	s_ashr_i32 s37, s36, 31
	s_lshl_b32 s27, s4, 5
	s_lshl_b64 s[38:39], s[36:37], 2
	v_mov_b32_e32 v69, 0
	s_mov_b32 s41, 0
	s_add_i32 s37, 0, 0x22200
	s_movk_i32 s53, 0x25f
	s_movk_i32 s54, 0x5c0
	v_mov_b32_e32 v72, 0x42000000
	v_mov_b32_e32 v73, 0x80
	s_branch .LBB0_69

.LBB0_140:
	s_mul_i32 s6, s47, 0x1fc
	s_bitset1_b32 s6, 10
	s_and_b64 s[4:5], s[4:5], exec
	s_cselect_b32 s10, s6, 0
	s_lshl_b32 s4, s47, 2
	s_mul_i32 s5, s4, s36
	s_and_b32 s9, s9, 0xffff
	s_add_i32 s6, s5, s4
	buffer_load_dwordx4 v[0:3], v71, s[8:11], s5 offen nt
	buffer_load_dwordx4 v[4:7], v71, s[8:11], s6 offen nt
	s_add_i32 s5, s6, s4
	s_add_i32 s6, s5, s4
	buffer_load_dwordx4 v[8:11], v71, s[8:11], s5 offen nt
	buffer_load_dwordx4 v[12:15], v71, s[8:11], s6 offen nt
	s_add_i32 s5, s6, s4
	s_add_i32 s6, s5, s4
	buffer_load_dwordx4 v[16:19], v71, s[8:11], s5 offen nt
	buffer_load_dwordx4 v[20:23], v71, s[8:11], s6 offen nt
	s_add_i32 s5, s6, s4
	s_add_i32 s6, s5, s4
	buffer_load_dwordx4 v[24:27], v71, s[8:11], s5 offen nt
	buffer_load_dwordx4 v[28:31], v71, s[8:11], s6 offen nt
	s_add_i32 s5, s6, s4
	s_add_i32 s6, s5, s4
	buffer_load_dwordx4 v[32:35], v71, s[8:11], s5 offen nt
	buffer_load_dwordx4 v[36:39], v71, s[8:11], s6 offen nt
	s_add_i32 s5, s6, s4
	s_add_i32 s6, s5, s4
	buffer_load_dwordx4 v[40:43], v71, s[8:11], s5 offen nt
	buffer_load_dwordx4 v[44:47], v71, s[8:11], s6 offen nt
	s_add_i32 s5, s6, s4
	s_add_i32 s6, s5, s4
	buffer_load_dwordx4 v[48:51], v71, s[8:11], s5 offen nt
	buffer_load_dwordx4 v[52:55], v71, s[8:11], s6 offen nt
	s_add_i32 s5, s6, s4
	s_add_i32 s4, s5, s4
	buffer_load_dwordx4 v[56:59], v71, s[8:11], s5 offen nt
	buffer_load_dwordx4 v[60:63], v71, s[8:11], s4 offen nt
	s_lshl_b32 s4, s73, 3
	s_add_i32 s4, s4, -1
	v_cmp_lt_i32_e64 s[6:7], s53, v64
	v_and_b32_e32 v64, s4, v70
	s_and_b64 s[4:5], s[44:45], exec
	s_cselect_b32 s4, 4, 3
	s_cselect_b32 s10, 8, 4
	s_cselect_b32 s44, 2, 3
	s_cmp_lg_u32 s29, 0
	s_cselect_b64 s[8:9], -1, 0
	s_ashr_i32 s5, s28, 31
	v_lshrrev_b32_e32 v65, s4, v70
	s_add_u32 s4, s34, s28
	v_lshlrev_b32_e32 v68, 4, v64
	s_addc_u32 s5, s35, s5
	s_mov_b32 s47, 0
	v_or_b32_e32 v65, s27, v65
	v_add_u32_e32 v64, 0, v68
	v_lshl_add_u64 v[66:67], s[4:5], 0, v[68:69]
	s_branch .LBB0_142
.LBB0_141:
	s_nop 0
	v_mad_u64_u32 v[76:77], s[4:5], v68, s55, v[64:65]
	ds_read_b128 v[76:79], v76
	v_ashrrev_i32_e32 v68, 31, v74
	v_mad_u64_u32 v[80:81], s[4:5], s30, v74, v[66:67]
	v_mul_lo_u32 v74, s31, v74
	v_mul_lo_u32 v68, s30, v68
	s_add_i32 s47, s28, 1
	v_add3_u32 v81, v74, v81, v68
	s_cmp_eq_u32 s47, s10
	s_waitcnt lgkmcnt(0)
	global_store_dwordx4 v[80:81], v[76:79], off sc1
	s_cbranch_scc1 .LBB0_68

.LBB0_144:
	v_mad_u64_u32 v[76:77], s[34:35], v68, s55, v[64:65]
	v_ashrrev_i32_e32 v68, 31, v74
	v_mad_u64_u32 v[80:81], s[34:35], s30, v74, v[66:67]
	s_add_i32 s28, s47, 1
	ds_read_b128 v[76:79], v76
	v_mul_lo_u32 v74, s31, v74
	v_mul_lo_u32 v68, s30, v68
	s_lshl_b32 s34, s28, s44
	v_add3_u32 v81, v74, v81, v68
	v_add_u32_e32 v68, s34, v65
	v_lshlrev_b32_e32 v74, 2, v68
	v_and_b32_e32 v74, 0xfc, v74
	v_ashrrev_i32_e32 v75, 6, v68
	s_and_b64 vcc, exec, s[4:5]
	v_add3_u32 v74, v75, s26, v74
	s_waitcnt lgkmcnt(0)
	global_store_dwordx4 v[80:81], v[76:79], off sc1
	s_cbranch_vccnz .LBB0_141
	v_mov_b32_e32 v75, s29
	v_cmp_gt_i32_e32 vcc, s29, v74
	s_nop 1
	v_cndmask_b32_e64 v75, v75, 0, vcc
	v_sub_u32_e32 v74, v74, v75
	v_lshlrev_b32_e32 v75, 1, v74
	v_and_b32_e32 v75, 0xffffff00, v75
	v_and_b32_e32 v74, 0x7f, v74
	v_cndmask_b32_e64 v76, v73, 0, vcc
	v_or3_b32 v74, v74, v76, v75
	s_branch .LBB0_141

.LBB0_1015:
	s_ashr_i32 s15, s28, 6
	s_mul_i32 s16, s22, 0x1fc
	s_add_i32 s82, s16, 0x400
	s_lshl_b32 s16, s15, 4
	s_lshl_b32 s17, s22, 2
	v_and_b32_e32 v70, 63, v0
	s_mul_i32 s18, s17, s16
	s_and_b32 s81, s81, 0xffff
	v_lshlrev_b32_e32 v71, 4, v70
	s_add_i32 s19, s18, s17
	buffer_load_dwordx4 v[0:3], v71, s[80:83], s18 offen nt
	buffer_load_dwordx4 v[4:7], v71, s[80:83], s19 offen nt
	s_add_i32 s18, s19, s17
	s_add_i32 s19, s18, s17
	buffer_load_dwordx4 v[8:11], v71, s[80:83], s18 offen nt
	buffer_load_dwordx4 v[12:15], v71, s[80:83], s19 offen nt
	s_add_i32 s18, s19, s17
	s_add_i32 s19, s18, s17
	buffer_load_dwordx4 v[16:19], v71, s[80:83], s18 offen nt
	buffer_load_dwordx4 v[20:23], v71, s[80:83], s19 offen nt
	s_add_i32 s18, s19, s17
	s_add_i32 s19, s18, s17
	buffer_load_dwordx4 v[24:27], v71, s[80:83], s18 offen nt
	buffer_load_dwordx4 v[28:31], v71, s[80:83], s19 offen nt
	s_add_i32 s18, s19, s17
	s_add_i32 s19, s18, s17
	buffer_load_dwordx4 v[32:35], v71, s[80:83], s18 offen nt
	buffer_load_dwordx4 v[36:39], v71, s[80:83], s19 offen nt
	s_add_i32 s18, s19, s17
	s_add_i32 s19, s18, s17
	buffer_load_dwordx4 v[40:43], v71, s[80:83], s18 offen nt
	buffer_load_dwordx4 v[44:47], v71, s[80:83], s19 offen nt
	s_add_i32 s18, s19, s17
	s_add_i32 s19, s18, s17
	buffer_load_dwordx4 v[48:51], v71, s[80:83], s18 offen nt
	buffer_load_dwordx4 v[52:55], v71, s[80:83], s19 offen nt
	s_add_i32 s18, s19, s17
	s_add_i32 s17, s18, s17
	buffer_load_dwordx4 v[56:59], v71, s[80:83], s18 offen nt
	buffer_load_dwordx4 v[60:63], v71, s[80:83], s17 offen nt
	s_lshl_b32 s15, s15, 5
	s_ashr_i32 s17, s16, 31
	s_branch .LBB0_1017

.LBB0_1089:
	s_mul_i32 s30, s41, 0x1fc
	s_addk_i32 s30, 0x400
	s_and_b64 s[24:25], s[24:25], exec
	s_cselect_b32 s82, s30, 0
	s_lshl_b32 s24, s41, 2
	s_mul_i32 s25, s24, s16
	s_and_b32 s81, s81, 0xffff
	s_add_i32 s30, s25, s24
	buffer_load_dwordx4 v[0:3], v71, s[80:83], s25 offen nt
	buffer_load_dwordx4 v[4:7], v71, s[80:83], s30 offen nt
	s_add_i32 s25, s30, s24
	s_add_i32 s30, s25, s24
	buffer_load_dwordx4 v[8:11], v71, s[80:83], s25 offen nt
	buffer_load_dwordx4 v[12:15], v71, s[80:83], s30 offen nt
	s_add_i32 s25, s30, s24
	s_add_i32 s30, s25, s24
	buffer_load_dwordx4 v[16:19], v71, s[80:83], s25 offen nt
	buffer_load_dwordx4 v[20:23], v71, s[80:83], s30 offen nt
	s_add_i32 s25, s30, s24
	s_add_i32 s30, s25, s24
	buffer_load_dwordx4 v[24:27], v71, s[80:83], s25 offen nt
	buffer_load_dwordx4 v[28:31], v71, s[80:83], s30 offen nt
	s_add_i32 s25, s30, s24
	s_add_i32 s30, s25, s24
	buffer_load_dwordx4 v[32:35], v71, s[80:83], s25 offen nt
	buffer_load_dwordx4 v[36:39], v71, s[80:83], s30 offen nt
	s_add_i32 s25, s30, s24
	s_add_i32 s30, s25, s24
	buffer_load_dwordx4 v[40:43], v71, s[80:83], s25 offen nt
	buffer_load_dwordx4 v[44:47], v71, s[80:83], s30 offen nt
	s_add_i32 s25, s30, s24
	s_add_i32 s30, s25, s24
	buffer_load_dwordx4 v[48:51], v71, s[80:83], s25 offen nt
	buffer_load_dwordx4 v[52:55], v71, s[80:83], s30 offen nt
	s_add_i32 s25, s30, s24
	s_add_i32 s24, s25, s24
	buffer_load_dwordx4 v[56:59], v71, s[80:83], s25 offen nt
	buffer_load_dwordx4 v[60:63], v71, s[80:83], s24 offen nt
	s_lshl_b32 s25, s36, 3
	s_add_i32 s25, s25, -1
	s_and_b64 s[18:19], s[18:19], exec
	v_cmp_le_i32_e64 s[40:41], s48, v64
	v_and_b32_e32 v64, s25, v70
	s_cselect_b32 s18, 4, 3
	s_cselect_b32 s25, 8, 4
	s_cselect_b32 s30, 2, 3
	s_cmp_lg_u32 s3, 0
	v_lshrrev_b32_e32 v65, s18, v70
	s_cselect_b64 s[18:19], -1, 0
	s_add_u32 s8, s8, s13
	s_addc_u32 s9, s9, 0
	v_lshlrev_b32_e32 v172, 4, v64
	s_cmp_eq_u32 s14, 2
	s_mov_b32 s24, 0
	v_or_b32_e32 v65, s15, v65
	v_add_u32_e32 v64, 0, v172
	v_lshl_add_u64 v[66:67], s[8:9], 0, v[172:173]
	s_cselect_b64 s[8:9], -1, 0
	s_branch .LBB0_1091

.LBB0_1093:
	v_mad_u64_u32 v[68:69], s[46:47], v68, s33, v[64:65]
	ds_read_b128 v[74:77], v68
	v_ashrrev_i32_e32 v73, 31, v72
	v_mad_u64_u32 v[68:69], s[46:47], s10, v72, v[66:67]
	v_mul_lo_u32 v72, s11, v72
	v_mul_lo_u32 v73, s10, v73
	v_add3_u32 v69, v72, v69, v73
	s_andn2_b64 vcc, exec, s[8:9]
	s_waitcnt lgkmcnt(0)
	global_store_dwordx4 v[68:69], v[74:77], off sc1
	s_cbranch_vccnz .LBB0_1090
	global_store_dwordx4 v[68:69], v[220:223], off offset:128 sc1
	s_branch .LBB0_1090

.LBB0_1472:
	s_lshl_b64 s[2:3], s[2:3], 2
	v_readlane_b32 s8, v254, 54
	v_readlane_b32 s24, v253, 14
	s_add_u32 s24, s8, s2
	v_readlane_b32 s2, v254, 55
	v_readlane_b32 s64, v252, 24
	s_addc_u32 s9, s2, s3
	s_ashr_i32 s2, s13, 6
	v_readlane_b32 s78, v252, 38
	v_readlane_b32 s79, v252, 39
	s_add_u32 s20, s78, 0x780000
	s_addc_u32 s21, s79, 0
	s_add_u32 s85, s78, 0x650000
	v_and_b32_e32 v128, 63, v132
	s_addc_u32 s86, s79, 0
	s_lshl_b32 s3, s2, 8
	v_or_b32_e32 v134, s3, v128
	v_bfe_u32 v142, v132, 3, 3
	v_lshlrev_b32_e32 v129, 2, v132
	v_readlane_b32 s10, v254, 56
	v_or_b32_e32 v2, 64, v134
	v_mul_u32_u24_e32 v0, 0x3000, v142
	v_and_b32_e32 v143, 28, v129
	v_ashrrev_i32_e32 v135, 31, v134
	v_readlane_b32 s11, v254, 57
	v_ashrrev_i32_e32 v3, 31, v2
	v_or_b32_e32 v4, v0, v143
	v_lshl_add_u64 v[0:1], v[134:135], 2, s[10:11]
	v_lshl_add_u64 v[2:3], v[2:3], 2, s[10:11]
	global_load_dword v1, v[0:1], off
	v_readlane_b32 s25, v253, 15
	global_load_dword v0, v[2:3], off
	v_or_b32_e32 v2, 0xc0, v134
	v_ashrrev_i32_e32 v3, 31, v2
	v_lshl_add_u64 v[2:3], v[2:3], 2, s[10:11]
	v_readlane_b32 s27, v253, 17
	s_mul_i32 s8, s2, 0xc00000
	v_readlane_b32 s26, v253, 16
	s_and_b32 s25, s9, 0xffff
	s_mov_b32 s27, s83
	s_or_b32 s9, s8, 0x60000
	v_cmp_gt_u32_e64 s[38:39], 8, v128
	v_lshlrev_b32_e32 v144, 4, v128
	v_lshlrev_b32_e32 v172, 3, v128
	v_and_b32_e32 v128, 64, v188
	v_or_b32_e32 v130, s3, v142
	v_mul_u32_u24_e32 v131, 0x1008, v143
	s_lshl_b32 s3, s2, 7
	s_lshl_b32 s88, s2, 10
	v_cmp_gt_i32_e64 s[40:41], 32, v132
	v_ashrrev_i32_e32 v133, 31, v132
	v_or_b32_e32 v159, 0x400, v144
	v_or_b32_e32 v160, 0x800, v144
	v_or_b32_e32 v161, 0xc00, v144
	v_readlane_b32 s65, v252, 25
	v_readlane_b32 s66, v252, 26
	v_readlane_b32 s67, v252, 27
	v_readlane_b32 s68, v252, 28
	v_readlane_b32 s69, v252, 29
	v_readlane_b32 s70, v252, 30
	v_readlane_b32 s71, v252, 31
	v_readlane_b32 s72, v252, 32
	v_readlane_b32 s73, v252, 33
	v_readlane_b32 s74, v252, 34
	v_readlane_b32 s75, v252, 35
	v_readlane_b32 s76, v252, 36
	v_readlane_b32 s77, v252, 37
	s_waitcnt vmcnt(0)
	v_pk_add_f32 v[138:139], v[0:1], 0 op_sel_hi:[1,0]
	v_or_b32_e32 v0, 0x80, v134
	v_ashrrev_i32_e32 v1, 31, v0
	v_lshl_add_u64 v[0:1], v[0:1], 2, s[10:11]
	global_load_dword v1, v[0:1], off
	s_mov_b32 s10, s26
	global_load_dword v0, v[2:3], off
	s_waitcnt vmcnt(0)
	v_pk_add_f32 v[136:137], v[0:1], 0 op_sel_hi:[1,0]
	v_lshlrev_b32_e32 v0, 2, v4
	buffer_load_dwordx4 v[124:127], v0, s[24:27], s8 offen nt
	buffer_load_dwordx4 v[120:123], v0, s[24:27], s9 offen nt
	s_or_b32 s9, s8, 0xc0000
	buffer_load_dwordx4 v[116:119], v0, s[24:27], s9 offen nt
	s_or_b32 s9, s8, 0x120000
	buffer_load_dwordx4 v[112:115], v0, s[24:27], s9 offen nt
	s_or_b32 s9, s8, 0x180000
	buffer_load_dwordx4 v[108:111], v0, s[24:27], s9 offen nt
	s_or_b32 s9, s8, 0x1e0000
	buffer_load_dwordx4 v[104:107], v0, s[24:27], s9 offen nt
	s_or_b32 s9, s8, 0x240000
	buffer_load_dwordx4 v[100:103], v0, s[24:27], s9 offen nt
	s_or_b32 s9, s8, 0x2a0000
	buffer_load_dwordx4 v[96:99], v0, s[24:27], s9 offen nt
	s_or_b32 s9, s8, 0x300000
	buffer_load_dwordx4 v[92:95], v0, s[24:27], s9 offen nt
	s_or_b32 s9, s8, 0x360000
	buffer_load_dwordx4 v[88:91], v0, s[24:27], s9 offen nt
	s_or_b32 s9, s8, 0x3c0000
	buffer_load_dwordx4 v[84:87], v0, s[24:27], s9 offen nt
	s_add_i32 s9, s8, 0x420000
	buffer_load_dwordx4 v[80:83], v0, s[24:27], s9 offen nt
	s_add_i32 s9, s8, 0x480000
	buffer_load_dwordx4 v[76:79], v0, s[24:27], s9 offen nt
	s_add_i32 s9, s8, 0x4e0000
	buffer_load_dwordx4 v[72:75], v0, s[24:27], s9 offen nt
	s_add_i32 s9, s8, 0x540000
	buffer_load_dwordx4 v[68:71], v0, s[24:27], s9 offen nt
	s_add_i32 s9, s8, 0x5a0000
	buffer_load_dwordx4 v[64:67], v0, s[24:27], s9 offen nt
	s_add_i32 s9, s8, 0x600000
	buffer_load_dwordx4 v[60:63], v0, s[24:27], s9 offen nt
	s_add_i32 s9, s8, 0x660000
	buffer_load_dwordx4 v[56:59], v0, s[24:27], s9 offen nt
	s_add_i32 s9, s8, 0x6c0000
	buffer_load_dwordx4 v[52:55], v0, s[24:27], s9 offen nt
	s_add_i32 s9, s8, 0x720000
	buffer_load_dwordx4 v[48:51], v0, s[24:27], s9 offen nt
	s_add_i32 s9, s8, 0x780000
	buffer_load_dwordx4 v[44:47], v0, s[24:27], s9 offen nt
	s_add_i32 s9, s8, 0x7e0000
	buffer_load_dwordx4 v[40:43], v0, s[24:27], s9 offen nt
	s_add_i32 s9, s8, 0x840000
	buffer_load_dwordx4 v[36:39], v0, s[24:27], s9 offen nt
	s_add_i32 s9, s8, 0x8a0000
	buffer_load_dwordx4 v[32:35], v0, s[24:27], s9 offen nt
	s_add_i32 s9, s8, 0x900000
	buffer_load_dwordx4 v[28:31], v0, s[24:27], s9 offen nt
	s_add_i32 s9, s8, 0x960000
	buffer_load_dwordx4 v[24:27], v0, s[24:27], s9 offen nt
	s_add_i32 s9, s8, 0x9c0000
	buffer_load_dwordx4 v[20:23], v0, s[24:27], s9 offen nt
	s_add_i32 s9, s8, 0xa20000
	buffer_load_dwordx4 v[16:19], v0, s[24:27], s9 offen nt
	s_add_i32 s9, s8, 0xa80000
	buffer_load_dwordx4 v[12:15], v0, s[24:27], s9 offen nt
	s_add_i32 s9, s8, 0xae0000
	buffer_load_dwordx4 v[8:11], v0, s[24:27], s9 offen nt
	s_add_i32 s9, s8, 0xb40000
	s_add_i32 s8, s8, 0xba0000
	buffer_load_dwordx4 v[4:7], v0, s[24:27], s9 offen nt
	v_writelane_b32 v253, s8, 14
	s_nop 1
	v_writelane_b32 v253, s9, 15
	v_writelane_b32 v253, s10, 16
	v_writelane_b32 v253, s11, 17
	buffer_load_dwordx4 v[0:3], v0, s[24:27], s8 offen nt
	v_readlane_b32 s8, v253, 7
	v_readlane_b32 s10, v253, 8
	s_add_i32 s87, s8, s3
	v_add_u32_e32 v145, s8, v129
	v_add_u32_e32 v146, s10, v129
	v_or_b32_e32 v129, v128, v142
	v_lshlrev_b32_e32 v147, 2, v129
	v_lshlrev_b32_e32 v129, 1, v130
	v_add3_u32 v148, 0, v131, v129
	v_xor_b32_e32 v129, 8, v188
	v_add_u32_e32 v128, 64, v128
	v_cmp_lt_i32_e32 vcc, v129, v128
	s_lshl_b32 s8, s2, 2
	s_lshl_b32 s3, s2, 4
	v_cndmask_b32_e32 v129, v188, v129, vcc
	s_mulk_i32 s2, 0x4020
	v_lshlrev_b32_e32 v156, 2, v129
	v_xor_b32_e32 v129, 16, v188
	s_add_i32 s91, s2, 0
	s_or_b32 s2, s8, 1
	v_cmp_lt_i32_e32 vcc, v129, v128
	s_ashr_i32 s9, s8, 31
	s_add_i32 s89, s10, s3
	s_ashr_i32 s3, s2, 31
	v_cndmask_b32_e32 v129, v188, v129, vcc
	s_lshl_b64 s[24:25], s[8:9], 11
	s_mul_i32 s9, s2, 0x1008
	s_lshl_b64 s[26:27], s[2:3], 11
	s_or_b32 s2, s8, 2
	v_lshlrev_b32_e32 v157, 2, v129
	v_xor_b32_e32 v129, 32, v188
	s_ashr_i32 s3, s2, 31
	v_cmp_lt_i32_e32 vcc, v129, v128
	s_lshl_b64 s[28:29], s[2:3], 11
	s_or_b32 s2, s8, 3
	v_cndmask_b32_e32 v128, v188, v129, vcc
	s_add_i32 s92, s9, 0
	s_ashr_i32 s3, s2, 31
	v_or_b32_e32 v149, 32, v147
	v_or_b32_e32 v150, 64, v147
	v_or_b32_e32 v151, 0x60, v147
	v_or_b32_e32 v152, 0x80, v147
	v_or_b32_e32 v153, 0xa0, v147
	v_or_b32_e32 v154, 0xc0, v147
	v_or_b32_e32 v155, 0xe0, v147
	v_lshlrev_b32_e32 v158, 2, v128
	s_add_i32 s93, s92, 0x1008
	s_add_i32 s95, s92, 0x2010
	s_lshl_b64 s[30:31], s[2:3], 11
	s_branch .LBB0_1474

.LBB0_1503:
	s_mul_i32 s12, s13, 0x1ffc
	s_bitset1_b32 s12, 7
	s_and_b64 s[2:3], s[2:3], exec
	s_cselect_b32 s82, s12, 0
	s_cmp_eq_u64 s[48:49], 0
	s_cselect_b64 s[2:3], -1, 0
	v_readlane_b32 s64, v252, 24
	s_and_b64 s[14:15], s[2:3], exec
	v_readlane_b32 s70, v252, 30
	v_readlane_b32 s71, v252, 31
	v_mul_u32_u24_e32 v0, s13, v142
	s_cselect_b32 s14, s71, s49
	s_cselect_b32 s15, s70, s48
	v_or_b32_e32 v2, v0, v143
	v_mov_b32_e32 v0, s15
	v_mov_b32_e32 v1, s14
	s_mul_i32 s12, s13, s88
	v_lshl_add_u64 v[0:1], v[134:135], 2, v[0:1]
	s_lshl_b32 s13, s13, 5
	global_load_dword v129, v[0:1], off
	global_load_dword v128, v[0:1], off offset:256
	global_load_dword v131, v[0:1], off offset:512
	global_load_dword v130, v[0:1], off offset:768
	s_and_b32 s81, s81, 0xffff
	v_lshlrev_b32_e32 v0, 2, v2
	s_add_i32 s14, s12, s13
	buffer_load_dwordx4 v[124:127], v0, s[80:83], s12 offen nt
	buffer_load_dwordx4 v[120:123], v0, s[80:83], s14 offen nt
	s_add_i32 s12, s14, s13
	s_add_i32 s14, s12, s13
	buffer_load_dwordx4 v[116:119], v0, s[80:83], s12 offen nt
	buffer_load_dwordx4 v[112:115], v0, s[80:83], s14 offen nt
	s_add_i32 s12, s14, s13
	s_add_i32 s14, s12, s13
	buffer_load_dwordx4 v[108:111], v0, s[80:83], s12 offen nt
	buffer_load_dwordx4 v[104:107], v0, s[80:83], s14 offen nt
	s_add_i32 s12, s14, s13
	s_add_i32 s14, s12, s13
	buffer_load_dwordx4 v[100:103], v0, s[80:83], s12 offen nt
	buffer_load_dwordx4 v[96:99], v0, s[80:83], s14 offen nt
	s_add_i32 s12, s14, s13
	s_add_i32 s14, s12, s13
	buffer_load_dwordx4 v[92:95], v0, s[80:83], s12 offen nt
	buffer_load_dwordx4 v[88:91], v0, s[80:83], s14 offen nt
	s_add_i32 s12, s14, s13
	s_add_i32 s14, s12, s13
	buffer_load_dwordx4 v[84:87], v0, s[80:83], s12 offen nt
	buffer_load_dwordx4 v[80:83], v0, s[80:83], s14 offen nt
	s_add_i32 s12, s14, s13
	s_add_i32 s14, s12, s13
	buffer_load_dwordx4 v[76:79], v0, s[80:83], s12 offen nt
	buffer_load_dwordx4 v[72:75], v0, s[80:83], s14 offen nt
	s_add_i32 s12, s14, s13
	s_add_i32 s14, s12, s13
	buffer_load_dwordx4 v[68:71], v0, s[80:83], s12 offen nt
	buffer_load_dwordx4 v[64:67], v0, s[80:83], s14 offen nt
	s_add_i32 s12, s14, s13
	s_add_i32 s14, s12, s13
	buffer_load_dwordx4 v[60:63], v0, s[80:83], s12 offen nt
	buffer_load_dwordx4 v[56:59], v0, s[80:83], s14 offen nt
	s_add_i32 s12, s14, s13
	s_add_i32 s14, s12, s13
	buffer_load_dwordx4 v[52:55], v0, s[80:83], s12 offen nt
	buffer_load_dwordx4 v[48:51], v0, s[80:83], s14 offen nt
	s_add_i32 s12, s14, s13
	s_add_i32 s14, s12, s13
	buffer_load_dwordx4 v[44:47], v0, s[80:83], s12 offen nt
	buffer_load_dwordx4 v[40:43], v0, s[80:83], s14 offen nt
	s_add_i32 s12, s14, s13
	s_add_i32 s14, s12, s13
	buffer_load_dwordx4 v[36:39], v0, s[80:83], s12 offen nt
	buffer_load_dwordx4 v[32:35], v0, s[80:83], s14 offen nt
	s_add_i32 s12, s14, s13
	s_add_i32 s14, s12, s13
	buffer_load_dwordx4 v[28:31], v0, s[80:83], s12 offen nt
	buffer_load_dwordx4 v[24:27], v0, s[80:83], s14 offen nt
	s_add_i32 s12, s14, s13
	s_add_i32 s14, s12, s13
	buffer_load_dwordx4 v[20:23], v0, s[80:83], s12 offen nt
	buffer_load_dwordx4 v[16:19], v0, s[80:83], s14 offen nt
	s_add_i32 s12, s14, s13
	s_add_i32 s14, s12, s13
	buffer_load_dwordx4 v[12:15], v0, s[80:83], s12 offen nt
	buffer_load_dwordx4 v[8:11], v0, s[80:83], s14 offen nt
	s_add_i32 s12, s14, s13
	s_add_i32 s13, s12, s13
	buffer_load_dwordx4 v[4:7], v0, s[80:83], s12 offen nt
	s_nop 0
	buffer_load_dwordx4 v[0:3], v0, s[80:83], s13 offen nt
	v_readlane_b32 s65, v252, 25
	v_readlane_b32 s66, v252, 26
	v_readlane_b32 s67, v252, 27
	v_readlane_b32 s68, v252, 28
	v_readlane_b32 s69, v252, 29
	v_readlane_b32 s72, v252, 32
	v_readlane_b32 s73, v252, 33
	v_readlane_b32 s74, v252, 34
	v_readlane_b32 s75, v252, 35
	v_readlane_b32 s76, v252, 36
	v_readlane_b32 s77, v252, 37
	v_readlane_b32 s78, v252, 38
	v_readlane_b32 s79, v252, 39
	s_and_saveexec_b64 s[44:45], s[40:41]
	s_cbranch_execz .LBB0_1473
	ds_read2_b32 v[136:137], v145 offset1:32
	s_mov_b32 s12, 0xda24260
	s_waitcnt lgkmcnt(0)
	v_max3_f32 v138, v136, s12, v137
	ds_read2_b32 v[136:137], v145 offset0:64 offset1:96
	s_waitcnt lgkmcnt(0)
	v_max3_f32 v138, v138, v136, v137
	ds_read2_b32 v[136:137], v145 offset0:128 offset1:160
	s_waitcnt lgkmcnt(0)
	v_max3_f32 v138, v138, v136, v137
	ds_read2_b32 v[136:137], v145 offset0:192 offset1:224
	s_waitcnt lgkmcnt(0)
	v_max3_f32 v136, v138, v136, v137
	ds_write_b32 v146, v136
	v_mul_f32_e32 v138, 0x3c010204, v136
	v_lshl_add_u64 v[136:137], v[132:133], 2, s[0:1]
	global_store_dword v[136:137], v138, off
	s_branch .LBB0_1473

.LBB0_1522:
	s_ashr_i32 s13, s13, 6
	s_mul_i32 s15, s16, 0x1fc
	s_add_i32 s82, s15, 0x400
	s_lshl_b32 s22, s13, 4
	s_lshl_b32 s15, s16, 2
	v_and_b32_e32 v70, 63, v0
	s_mul_i32 s16, s15, s22
	s_and_b32 s81, s81, 0xffff
	v_lshlrev_b32_e32 v71, 4, v70
	s_add_i32 s17, s16, s15
	buffer_load_dwordx4 v[0:3], v71, s[80:83], s16 offen nt
	buffer_load_dwordx4 v[4:7], v71, s[80:83], s17 offen nt
	s_add_i32 s16, s17, s15
	s_add_i32 s17, s16, s15
	buffer_load_dwordx4 v[8:11], v71, s[80:83], s16 offen nt
	buffer_load_dwordx4 v[12:15], v71, s[80:83], s17 offen nt
	s_add_i32 s16, s17, s15
	s_add_i32 s17, s16, s15
	buffer_load_dwordx4 v[16:19], v71, s[80:83], s16 offen nt
	buffer_load_dwordx4 v[20:23], v71, s[80:83], s17 offen nt
	s_add_i32 s16, s17, s15
	s_add_i32 s17, s16, s15
	buffer_load_dwordx4 v[24:27], v71, s[80:83], s16 offen nt
	buffer_load_dwordx4 v[28:31], v71, s[80:83], s17 offen nt
	s_add_i32 s16, s17, s15
	s_add_i32 s17, s16, s15
	buffer_load_dwordx4 v[32:35], v71, s[80:83], s16 offen nt
	buffer_load_dwordx4 v[36:39], v71, s[80:83], s17 offen nt
	s_add_i32 s16, s17, s15
	s_add_i32 s17, s16, s15
	buffer_load_dwordx4 v[40:43], v71, s[80:83], s16 offen nt
	buffer_load_dwordx4 v[44:47], v71, s[80:83], s17 offen nt
	s_add_i32 s16, s17, s15
	s_add_i32 s17, s16, s15
	buffer_load_dwordx4 v[48:51], v71, s[80:83], s16 offen nt
	buffer_load_dwordx4 v[52:55], v71, s[80:83], s17 offen nt
	s_add_i32 s16, s17, s15
	s_add_i32 s15, s16, s15
	buffer_load_dwordx4 v[56:59], v71, s[80:83], s16 offen nt
	buffer_load_dwordx4 v[60:63], v71, s[80:83], s15 offen nt
	s_lshl_b32 s13, s13, 5
	s_ashr_i32 s23, s22, 31
	s_branch .LBB0_1524

.LBB0_1593:
	s_mul_i32 s14, s20, 0x1fc
	s_addk_i32 s14, 0x400
	s_and_b64 s[38:39], s[38:39], exec
	s_cselect_b32 s82, s14, 0
	s_lshl_b32 s14, s20, 2
	s_mul_i32 s20, s14, s22
	s_and_b32 s81, s81, 0xffff
	s_add_i32 s21, s20, s14
	buffer_load_dwordx4 v[0:3], v71, s[80:83], s20 offen nt
	buffer_load_dwordx4 v[4:7], v71, s[80:83], s21 offen nt
	s_add_i32 s20, s21, s14
	s_add_i32 s21, s20, s14
	buffer_load_dwordx4 v[8:11], v71, s[80:83], s20 offen nt
	buffer_load_dwordx4 v[12:15], v71, s[80:83], s21 offen nt
	s_add_i32 s20, s21, s14
	s_add_i32 s21, s20, s14
	buffer_load_dwordx4 v[16:19], v71, s[80:83], s20 offen nt
	buffer_load_dwordx4 v[20:23], v71, s[80:83], s21 offen nt
	s_add_i32 s20, s21, s14
	s_add_i32 s21, s20, s14
	buffer_load_dwordx4 v[24:27], v71, s[80:83], s20 offen nt
	buffer_load_dwordx4 v[28:31], v71, s[80:83], s21 offen nt
	s_add_i32 s20, s21, s14
	s_add_i32 s21, s20, s14
	buffer_load_dwordx4 v[32:35], v71, s[80:83], s20 offen nt
	buffer_load_dwordx4 v[36:39], v71, s[80:83], s21 offen nt
	s_add_i32 s20, s21, s14
	s_add_i32 s21, s20, s14
	buffer_load_dwordx4 v[40:43], v71, s[80:83], s20 offen nt
	buffer_load_dwordx4 v[44:47], v71, s[80:83], s21 offen nt
	s_add_i32 s20, s21, s14
	s_add_i32 s21, s20, s14
	buffer_load_dwordx4 v[48:51], v71, s[80:83], s20 offen nt
	buffer_load_dwordx4 v[52:55], v71, s[80:83], s21 offen nt
	s_add_i32 s20, s21, s14
	s_add_i32 s14, s20, s14
	buffer_load_dwordx4 v[56:59], v71, s[80:83], s20 offen nt
	buffer_load_dwordx4 v[60:63], v71, s[80:83], s14 offen nt
	s_lshl_b32 s16, s16, 3
	s_add_i32 s16, s16, -1
	s_movk_i32 s14, 0x3bf
	s_and_b64 s[20:21], s[24:25], exec
	v_cmp_lt_i32_e64 s[38:39], s14, v64
	v_and_b32_e32 v64, s16, v70
	s_cselect_b32 s16, 4, 3
	v_lshrrev_b32_e32 v65, s16, v70
	s_cselect_b32 s16, 8, 4
	s_cselect_b32 s20, 2, 3
	s_cmp_lg_u32 s3, 0
	s_cselect_b64 s[24:25], -1, 0
	s_add_u32 s8, s8, s7
	s_addc_u32 s9, s9, 0
	v_lshlrev_b32_e32 v172, 4, v64
	s_cmp_eq_u32 s12, 2
	s_mov_b32 s14, 0
	v_or_b32_e32 v65, s13, v65
	v_add_u32_e32 v64, 0, v172
	v_lshl_add_u64 v[66:67], s[8:9], 0, v[172:173]
	s_cselect_b64 s[8:9], -1, 0
	s_branch .LBB0_1595

.LBB0_1597:
	v_mad_u64_u32 v[68:69], s[44:45], v68, s15, v[64:65]
	ds_read_b128 v[74:77], v68
	v_ashrrev_i32_e32 v73, 31, v72
	v_mad_u64_u32 v[68:69], s[44:45], s10, v72, v[66:67]
	v_mul_lo_u32 v72, s11, v72
	v_mul_lo_u32 v73, s10, v73
	v_add3_u32 v69, v72, v69, v73
	s_andn2_b64 vcc, exec, s[8:9]
	s_waitcnt lgkmcnt(0)
	global_store_dwordx4 v[68:69], v[74:77], off sc1
	s_cbranch_vccnz .LBB0_1594
	global_store_dwordx4 v[68:69], v[220:223], off offset:128 sc1
	s_branch .LBB0_1594

.LBB0_1722:
	s_ashr_i32 s13, s13, 6
	s_mul_i32 s14, s11, 0x1fc
	s_lshl_b32 s28, s13, 4
	s_lshl_b32 s11, s11, 2
	v_and_b32_e32 v70, 63, v0
	s_or_b32 s82, s14, 0x400
	s_mul_i32 s14, s11, s28
	s_and_b32 s81, s81, 0xffff
	v_lshlrev_b32_e32 v71, 4, v70
	s_add_i32 s15, s14, s11
	buffer_load_dwordx4 v[0:3], v71, s[80:83], s14 offen nt
	buffer_load_dwordx4 v[4:7], v71, s[80:83], s15 offen nt
	s_add_i32 s14, s15, s11
	s_add_i32 s15, s14, s11
	buffer_load_dwordx4 v[8:11], v71, s[80:83], s14 offen nt
	buffer_load_dwordx4 v[12:15], v71, s[80:83], s15 offen nt
	s_add_i32 s14, s15, s11
	s_add_i32 s15, s14, s11
	buffer_load_dwordx4 v[16:19], v71, s[80:83], s14 offen nt
	buffer_load_dwordx4 v[20:23], v71, s[80:83], s15 offen nt
	s_add_i32 s14, s15, s11
	s_add_i32 s15, s14, s11
	buffer_load_dwordx4 v[24:27], v71, s[80:83], s14 offen nt
	buffer_load_dwordx4 v[28:31], v71, s[80:83], s15 offen nt
	s_add_i32 s14, s15, s11
	s_add_i32 s15, s14, s11
	buffer_load_dwordx4 v[32:35], v71, s[80:83], s14 offen nt
	buffer_load_dwordx4 v[36:39], v71, s[80:83], s15 offen nt
	s_add_i32 s14, s15, s11
	s_add_i32 s15, s14, s11
	buffer_load_dwordx4 v[40:43], v71, s[80:83], s14 offen nt
	buffer_load_dwordx4 v[44:47], v71, s[80:83], s15 offen nt
	s_add_i32 s14, s15, s11
	s_add_i32 s15, s14, s11
	buffer_load_dwordx4 v[48:51], v71, s[80:83], s14 offen nt
	buffer_load_dwordx4 v[52:55], v71, s[80:83], s15 offen nt
	s_add_i32 s14, s15, s11
	s_add_i32 s11, s14, s11
	buffer_load_dwordx4 v[56:59], v71, s[80:83], s14 offen nt
	buffer_load_dwordx4 v[60:63], v71, s[80:83], s11 offen nt
	s_lshl_b32 s11, s13, 5
	s_ashr_i32 s29, s28, 31
	s_branch .LBB0_1724

.LBB0_1802:
	s_mul_i32 s16, s19, 0x1fc
	s_bitset1_b32 s16, 10
	s_and_b64 s[20:21], s[36:37], exec
	s_cselect_b32 s82, s16, 0
	s_lshl_b32 s16, s19, 2
	s_mul_i32 s19, s16, s28
	s_and_b32 s81, s81, 0xffff
	s_add_i32 s20, s19, s16
	buffer_load_dwordx4 v[0:3], v71, s[80:83], s19 offen nt
	buffer_load_dwordx4 v[4:7], v71, s[80:83], s20 offen nt
	s_add_i32 s19, s20, s16
	s_add_i32 s20, s19, s16
	buffer_load_dwordx4 v[8:11], v71, s[80:83], s19 offen nt
	buffer_load_dwordx4 v[12:15], v71, s[80:83], s20 offen nt
	s_add_i32 s19, s20, s16
	s_add_i32 s20, s19, s16
	buffer_load_dwordx4 v[16:19], v71, s[80:83], s19 offen nt
	buffer_load_dwordx4 v[20:23], v71, s[80:83], s20 offen nt
	s_add_i32 s19, s20, s16
	s_add_i32 s20, s19, s16
	buffer_load_dwordx4 v[24:27], v71, s[80:83], s19 offen nt
	buffer_load_dwordx4 v[28:31], v71, s[80:83], s20 offen nt
	s_add_i32 s19, s20, s16
	s_add_i32 s20, s19, s16
	buffer_load_dwordx4 v[32:35], v71, s[80:83], s19 offen nt
	buffer_load_dwordx4 v[36:39], v71, s[80:83], s20 offen nt
	s_add_i32 s19, s20, s16
	s_add_i32 s20, s19, s16
	buffer_load_dwordx4 v[40:43], v71, s[80:83], s19 offen nt
	buffer_load_dwordx4 v[44:47], v71, s[80:83], s20 offen nt
	s_add_i32 s19, s20, s16
	s_add_i32 s20, s19, s16
	buffer_load_dwordx4 v[48:51], v71, s[80:83], s19 offen nt
	buffer_load_dwordx4 v[52:55], v71, s[80:83], s20 offen nt
	s_add_i32 s19, s20, s16
	s_add_i32 s16, s19, s16
	buffer_load_dwordx4 v[56:59], v71, s[80:83], s19 offen nt
	buffer_load_dwordx4 v[60:63], v71, s[80:83], s16 offen nt
	s_lshl_b32 s14, s14, 3
	s_add_i32 s14, s14, -1
	s_movk_i32 s16, 0x6ff
	s_and_b64 s[20:21], s[38:39], exec
	v_cmp_lt_i32_e64 s[36:37], s16, v64
	v_and_b32_e32 v64, s14, v70
	s_cselect_b32 s14, 4, 3
	v_lshrrev_b32_e32 v65, s14, v70
	s_cselect_b32 s14, 8, 4
	s_cselect_b32 s16, 2, 3
	s_cmp_lg_u32 s7, 0
	s_cselect_b64 s[38:39], -1, 0
	s_ashr_i32 s19, s8, 31
	s_add_u32 s20, s26, s8
	s_addc_u32 s21, s27, s19
	v_lshlrev_b32_e32 v172, 4, v64
	s_cmp_eq_u32 s9, 2
	v_or_b32_e32 v65, s11, v65
	v_add_u32_e32 v64, 0, v172
	v_lshl_add_u64 v[66:67], s[20:21], 0, v[172:173]
	s_cselect_b64 s[8:9], -1, 0
	s_branch .LBB0_1804

.LBB0_1806:
	v_mad_u64_u32 v[68:69], s[20:21], v68, s13, v[64:65]
	ds_read_b128 v[74:77], v68
	v_ashrrev_i32_e32 v73, 31, v72
	v_mad_u64_u32 v[68:69], s[20:21], s24, v72, v[66:67]
	v_mul_lo_u32 v72, s25, v72
	v_mul_lo_u32 v73, s24, v73
	v_add3_u32 v69, v72, v69, v73
	s_andn2_b64 vcc, exec, s[8:9]
	s_waitcnt lgkmcnt(0)
	global_store_dwordx4 v[68:69], v[74:77], off sc1
	s_cbranch_vccnz .LBB0_1803
	global_store_dwordx4 v[68:69], v[220:223], off offset:128 sc1
	s_branch .LBB0_1803
